# deferred conversion: 5 items per wave in the P5 and P14 idle slots (24.6% of the MoE conversion)
# baseline (speedup 1.0000x reference)
; #define LAS __attribute__((address_space(3)))
; __device__ __forceinline__ int tidx() { int t = threadIdx.x; asm volatile("" : "+v"(t)); return t; }
; __device__ __forceinline__ void phase_cvt_moe(LAS unsigned char* lds, const CvtMoe a) {
;     const int tid_ = tidx(), wave = tid_ >> 6, lane = tid_ & 63;
;     LAS float* scr = (LAS float*)(lds + wave * CVT_SCR);
;     const int gw = blockIdx.x * 8 + wave, NGW = gridDim.x * 8;
;     constexpr int IG = (D / 64) * (FF / 64), ID = (FF / 64) * (D / 64);
;     for (int it = gw; it < 2 * NE * (2 * IG + ID); it += NGW) {
;         const int e = it / (2 * IG + ID); int r = it % (2 * IG + ID);
;         if (r < 2 * IG) { const int up = r / IG; r %= IG; const int nblk = FF / 64, kb = r / nblk, nb = r % nblk, n0 = nb * 64;
;             cvt_item((up ? a.wu : a.wg) + (size_t)e * D * FF, D, FF, a.gu + (size_t)e * 2 * FF * D, (n0 / 128) * 256 + up * 128 + (n0 % 128), kb * 64, n0, scr, lane); }
;         else { r -= 2 * IG; const int nblk = D / 64, kb = r / nblk, nb = r % nblk; cvt_item(a.wd + (size_t)e * FF * D, FF, D, a.dn + (size_t)e * D * FF, nb * 64, kb * 64, nb * 64, scr, lane); }
;     }
.LBB0_55:
	s_or_b64 exec, exec, s[4:5]
	s_add_u32 s4, s90, 0x30a13600
	s_addc_u32 s5, s91, 0
	v_writelane_b32 v250, s4, 6
	v_mov_b32_e32 v4, v0
	s_nop 0
	v_writelane_b32 v250, s5, 7
	s_add_u32 s4, s90, 0x46a13600
	s_addc_u32 s5, s91, 0
	v_writelane_b32 v250, s4, 8
	v_ashrrev_i32_e32 v2, 6, v4
	v_add_u32_e32 v5, s14, v2
	v_writelane_b32 v250, s5, 9
	s_mov_b32 s4, 0xc700
	v_cmp_gt_i32_e32 vcc, s4, v5
	s_and_saveexec_b64 s[4:5], vcc
	s_cbranch_execz .LBB0_62
	s_movk_i32 s6, 0x4100
	v_mul_lo_u32 v3, v2, s6
	v_add_u32_e32 v8, 0, v3
	v_lshlrev_b32_e32 v3, 2, v4
	v_bfe_u32 v6, v4, 4, 2
	v_and_b32_e32 v44, 60, v3
	v_bfe_u32 v7, v4, 3, 3
	v_lshlrev_b32_e32 v4, 3, v4
	v_lshl_add_u32 v20, v44, 2, v8
	v_mul_u32_u24_e32 v21, 0x104, v6
	v_and_b32_e32 v4, 56, v4
	v_mul_u32_u24_e32 v9, 0x104, v4
	v_lshlrev_b32_e32 v10, 2, v7
	v_lshlrev_b32_e32 v16, 2, v2
	v_add_u32_e32 v20, v20, v21
	v_mov_b32_e32 v3, 0
	v_add3_u32 v8, v8, v9, v10
	v_or_b32_e32 v9, 8, v7
	v_or_b32_e32 v10, 16, v7
	v_or_b32_e32 v11, 24, v7
	v_or_b32_e32 v12, 32, v7
	v_or_b32_e32 v13, 40, v7
	v_or_b32_e32 v14, 48, v7
	v_or_b32_e32 v15, 56, v7
	v_lshl_add_u32 v16, s2, 5, v16
	v_lshlrev_b32_e32 v17, 2, v1
	v_lshl_add_u32 v18, v2, 6, s3
	v_lshlrev_b32_e32 v19, 6, v1
	s_mov_b64 s[6:7], 0
	s_mov_b32 s3, 0x3e0f83e1
	s_movk_i32 s10, 0x57f
	s_mov_b32 s11, 0xb00000
	v_add_u32_e32 v21, 0x410, v20
	v_add_u32_e32 v22, 0x418, v20
	v_add_u32_e32 v23, 0x820, v20
	v_add_u32_e32 v24, 0x828, v20
	v_add_u32_e32 v25, 0xc30, v20
	v_add_u32_e32 v26, 0xc38, v20
	v_add_u32_e32 v27, 0x1040, v20
	v_add_u32_e32 v28, 0x1048, v20
	v_add_u32_e32 v29, 0x1450, v20
	v_add_u32_e32 v30, 0x1458, v20
	v_add_u32_e32 v31, 0x1860, v20
	v_add_u32_e32 v32, 0x1868, v20
	v_add_u32_e32 v33, 0x1c70, v20
	v_add_u32_e32 v34, 0x1c78, v20
	v_add_u32_e32 v35, 0x2080, v20
	v_add_u32_e32 v36, 0x2088, v20
	v_add_u32_e32 v37, 0x2490, v20
	v_add_u32_e32 v38, 0x2498, v20
	v_add_u32_e32 v39, 0x28a0, v20
	v_add_u32_e32 v40, 0x28a8, v20
	v_add_u32_e32 v41, 0x2cb0, v20
	v_add_u32_e32 v42, 0x2cb8, v20
	s_movk_i32 s12, 0xba3
	s_mov_b32 s13, 0xb000
	s_mov_b32 s14, 0x16000
	s_mov_b32 s15, 0x21000
	s_mov_b32 s16, 0x2c000
	s_mov_b32 s17, 0x37000
	s_mov_b32 s18, 0x42000
	s_mov_b32 s19, 0x4d000
	s_mov_b32 s20, 0x58000
	s_mov_b32 s21, 0x63000
	s_mov_b32 s22, 0x6e000
	s_mov_b32 s23, 0x79000
	s_mov_b32 s24, 0x84000
	s_mov_b32 s25, 0x8f000
	s_mov_b32 s26, 0x9a000
	s_mov_b32 s27, 0xa5000
	s_mov_b32 s28, 0xc6ff
	v_lshlrev_b32_e32 v2, 2, v44
	v_add_u32_e32 v43, 0x30c0, v20
	v_add_u32_e32 v44, 0x30c8, v20
	v_add_u32_e32 v45, 0x34d0, v20
	v_add_u32_e32 v46, 0x34d8, v20
	v_mov_b32_e32 v47, 6
	v_mov_b32_e32 v48, 1
	v_mov_b32_e32 v49, 8
	v_mov_b32_e32 v50, 7
	s_branch .LBB0_58

; #define LAS __attribute__((address_space(3)))
; __device__ __forceinline__ int tidx() { int t = threadIdx.x; asm volatile("" : "+v"(t)); return t; }
; __device__ __forceinline__ void phase_cvt_moe(LAS unsigned char* lds, const CvtMoe a) {
;     const int tid_ = tidx(), wave = tid_ >> 6, lane = tid_ & 63;
;     LAS float* scr = (LAS float*)(lds + wave * CVT_SCR);
;     const int gw = blockIdx.x * 8 + wave, NGW = gridDim.x * 8;
;     constexpr int IG = (D / 64) * (FF / 64), ID = (FF / 64) * (D / 64);
;     for (int it = gw; it < 2 * NE * (2 * IG + ID); it += NGW) {
;         const int e = it / (2 * IG + ID); int r = it % (2 * IG + ID);
;         if (r < 2 * IG) { const int up = r / IG; r %= IG; const int nblk = FF / 64, kb = r / nblk, nb = r % nblk, n0 = nb * 64;
.Lcvp5_entry:
	s_sub_i32 s0, s94, 64
	v_readlane_b32 s2, v250, 26
	v_readlane_b32 s3, v250, 27
	s_nop 3
	s_sub_u32 s2, s2, 0xc0
	s_subb_u32 s3, s3, 0
	s_load_dwordx2 s[38:39], s[2:3], 0x90
	s_load_dwordx2 s[40:41], s[2:3], 0x98
	s_load_dwordx2 s[34:35], s[2:3], 0xa0
	s_lshl_b32 s0, s0, 3
	s_add_i32 s0, s0, 0xc700
	v_mov_b32_e32 v131, 0x600
	s_waitcnt lgkmcnt(0)
	s_add_u32 s4, s90, 0x30a13600
	s_addc_u32 s5, s91, 0
	v_writelane_b32 v250, s4, 6
	v_mov_b32_e32 v130, v0
	s_nop 0
	v_writelane_b32 v250, s5, 7
	s_add_u32 s4, s90, 0x46a13600
	s_addc_u32 s5, s91, 0
	v_writelane_b32 v250, s4, 8
	v_ashrrev_i32_e32 v2, 6, v130
	v_add_u32_e32 v5, s0, v2
	v_writelane_b32 v250, s5, 9
	s_mov_b32 s4, 0xe500
	v_cmp_gt_i32_e32 vcc, s4, v5
	s_and_saveexec_b64 s[4:5], vcc
	s_cbranch_execz .Lcvp5_62
	s_movk_i32 s6, 0x4100
	v_mul_lo_u32 v3, v2, s6
	v_add_u32_e32 v8, 0, v3
	v_lshlrev_b32_e32 v3, 2, v130
	v_bfe_u32 v6, v130, 4, 2
	v_and_b32_e32 v44, 60, v3
	v_bfe_u32 v7, v130, 3, 3
	v_lshlrev_b32_e32 v130, 3, v130
	v_lshl_add_u32 v20, v44, 2, v8
	v_mul_u32_u24_e32 v21, 0x104, v6
	v_and_b32_e32 v130, 56, v130
	v_mul_u32_u24_e32 v9, 0x104, v130
	v_lshlrev_b32_e32 v10, 2, v7
	v_lshlrev_b32_e32 v16, 2, v2
	v_add_u32_e32 v20, v20, v21
	v_mov_b32_e32 v3, 0
	v_add3_u32 v8, v8, v9, v10
	v_or_b32_e32 v9, 8, v7
	v_or_b32_e32 v10, 16, v7
	v_or_b32_e32 v11, 24, v7
	v_or_b32_e32 v12, 32, v7
	v_or_b32_e32 v13, 40, v7
	v_or_b32_e32 v14, 48, v7
	v_or_b32_e32 v15, 56, v7
	v_lshlrev_b32_e32 v16, 2, v5
	v_lshlrev_b32_e32 v17, 2, v131
	v_lshlrev_b32_e32 v18, 6, v5
	v_lshlrev_b32_e32 v19, 6, v131
	s_mov_b64 s[6:7], 0
	s_mov_b32 s3, 0x3e0f83e1
	s_movk_i32 s10, 0x57f
	s_mov_b32 s11, 0xb00000
	v_add_u32_e32 v21, 0x410, v20
	v_add_u32_e32 v22, 0x418, v20
	v_add_u32_e32 v23, 0x820, v20
	v_add_u32_e32 v24, 0x828, v20
	v_add_u32_e32 v25, 0xc30, v20
	v_add_u32_e32 v26, 0xc38, v20
	v_add_u32_e32 v27, 0x1040, v20
	v_add_u32_e32 v28, 0x1048, v20
	v_add_u32_e32 v29, 0x1450, v20
	v_add_u32_e32 v30, 0x1458, v20
	v_add_u32_e32 v31, 0x1860, v20
	v_add_u32_e32 v32, 0x1868, v20
	v_add_u32_e32 v33, 0x1c70, v20
	v_add_u32_e32 v34, 0x1c78, v20
	v_add_u32_e32 v35, 0x2080, v20
	v_add_u32_e32 v36, 0x2088, v20
	v_add_u32_e32 v37, 0x2490, v20
	v_add_u32_e32 v38, 0x2498, v20
	v_add_u32_e32 v39, 0x28a0, v20
	v_add_u32_e32 v40, 0x28a8, v20
	v_add_u32_e32 v41, 0x2cb0, v20
	v_add_u32_e32 v42, 0x2cb8, v20
	s_movk_i32 s64, 0xba3
	s_mov_b32 s65, 0xb000
	s_mov_b32 s66, 0x16000
	s_mov_b32 s67, 0x21000
	s_mov_b32 s16, 0x2c000
	s_mov_b32 s68, 0x37000
	s_mov_b32 s69, 0x42000
	s_mov_b32 s19, 0x4d000
	s_mov_b32 s20, 0x58000
	s_mov_b32 s21, 0x63000
	s_mov_b32 s70, 0x6e000
	s_mov_b32 s23, 0x79000
	s_mov_b32 s24, 0x84000
	s_mov_b32 s25, 0x8f000
	s_mov_b32 s26, 0x9a000
	s_mov_b32 s27, 0xa5000
	s_mov_b32 s71, 0xe4ff
	v_lshlrev_b32_e32 v2, 2, v44
	v_add_u32_e32 v43, 0x30c0, v20
	v_add_u32_e32 v44, 0x30c8, v20
	v_add_u32_e32 v45, 0x34d0, v20
	v_add_u32_e32 v46, 0x34d8, v20
	v_mov_b32_e32 v47, 6
	v_mov_b32_e32 v132, 1
	v_mov_b32_e32 v133, 8
	v_mov_b32_e32 v134, 7
	s_branch .Lcvp5_58

; #define LAS __attribute__((address_space(3)))
; __device__ __forceinline__ int tidx() { int t = threadIdx.x; asm volatile("" : "+v"(t)); return t; }
; __device__ __forceinline__ void phase_cvt_moe(LAS unsigned char* lds, const CvtMoe a) {
;     const int tid_ = tidx(), wave = tid_ >> 6, lane = tid_ & 63;
;     LAS float* scr = (LAS float*)(lds + wave * CVT_SCR);
;     const int gw = blockIdx.x * 8 + wave, NGW = gridDim.x * 8;
;     constexpr int IG = (D / 64) * (FF / 64), ID = (FF / 64) * (D / 64);
;     for (int it = gw; it < 2 * NE * (2 * IG + ID); it += NGW) {
;         const int e = it / (2 * IG + ID); int r = it % (2 * IG + ID);
;         if (r < 2 * IG) { const int up = r / IG; r %= IG; const int nblk = FF / 64, kb = r / nblk, nb = r % nblk, n0 = nb * 64;
.Lcvp14_entry:
	s_sub_i32 s0, s94, 32
	v_readlane_b32 s2, v250, 26
	v_readlane_b32 s3, v250, 27
	s_nop 3
	s_sub_u32 s2, s2, 0xc0
	s_subb_u32 s3, s3, 0
	s_load_dwordx2 s[38:39], s[2:3], 0x90
	s_load_dwordx2 s[40:41], s[2:3], 0x98
	s_load_dwordx2 s[34:35], s[2:3], 0xa0
	s_lshl_b32 s0, s0, 3
	s_add_i32 s0, s0, 0xe500
	v_mov_b32_e32 v131, 0x700
	s_waitcnt lgkmcnt(0)
	s_add_u32 s4, s90, 0x30a13600
	s_addc_u32 s5, s91, 0
	v_writelane_b32 v250, s4, 6
	v_mov_b32_e32 v130, v0
	s_nop 0
	v_writelane_b32 v250, s5, 7
	s_add_u32 s4, s90, 0x46a13600
	s_addc_u32 s5, s91, 0
	v_writelane_b32 v250, s4, 8
	v_ashrrev_i32_e32 v2, 6, v130
	v_add_u32_e32 v5, s0, v2
	v_writelane_b32 v250, s5, 9
	s_mov_b32 s4, 0x10800
	v_cmp_gt_i32_e32 vcc, s4, v5
	s_and_saveexec_b64 s[4:5], vcc
	s_cbranch_execz .Lcvp14_62
	s_movk_i32 s6, 0x4100
	v_mul_lo_u32 v3, v2, s6
	v_add_u32_e32 v8, 0, v3
	v_lshlrev_b32_e32 v3, 2, v130
	v_bfe_u32 v6, v130, 4, 2
	v_and_b32_e32 v44, 60, v3
	v_bfe_u32 v7, v130, 3, 3
	v_lshlrev_b32_e32 v130, 3, v130
	v_lshl_add_u32 v20, v44, 2, v8
	v_mul_u32_u24_e32 v21, 0x104, v6
	v_and_b32_e32 v130, 56, v130
	v_mul_u32_u24_e32 v9, 0x104, v130
	v_lshlrev_b32_e32 v10, 2, v7
	v_lshlrev_b32_e32 v16, 2, v2
	v_add_u32_e32 v20, v20, v21
	v_mov_b32_e32 v3, 0
	v_add3_u32 v8, v8, v9, v10
	v_or_b32_e32 v9, 8, v7
	v_or_b32_e32 v10, 16, v7
	v_or_b32_e32 v11, 24, v7
	v_or_b32_e32 v12, 32, v7
	v_or_b32_e32 v13, 40, v7
	v_or_b32_e32 v14, 48, v7
	v_or_b32_e32 v15, 56, v7
	v_lshlrev_b32_e32 v16, 2, v5
	v_lshlrev_b32_e32 v17, 2, v131
	v_lshlrev_b32_e32 v18, 6, v5
	v_lshlrev_b32_e32 v19, 6, v131
	s_mov_b64 s[6:7], 0
	s_mov_b32 s3, 0x3e0f83e1
	s_movk_i32 s10, 0x57f
	s_mov_b32 s11, 0xb00000
	v_add_u32_e32 v21, 0x410, v20
	v_add_u32_e32 v22, 0x418, v20
	v_add_u32_e32 v23, 0x820, v20
	v_add_u32_e32 v24, 0x828, v20
	v_add_u32_e32 v25, 0xc30, v20
	v_add_u32_e32 v26, 0xc38, v20
	v_add_u32_e32 v27, 0x1040, v20
	v_add_u32_e32 v28, 0x1048, v20
	v_add_u32_e32 v29, 0x1450, v20
	v_add_u32_e32 v30, 0x1458, v20
	v_add_u32_e32 v31, 0x1860, v20
	v_add_u32_e32 v32, 0x1868, v20
	v_add_u32_e32 v33, 0x1c70, v20
	v_add_u32_e32 v34, 0x1c78, v20
	v_add_u32_e32 v35, 0x2080, v20
	v_add_u32_e32 v36, 0x2088, v20
	v_add_u32_e32 v37, 0x2490, v20
	v_add_u32_e32 v38, 0x2498, v20
	v_add_u32_e32 v39, 0x28a0, v20
	v_add_u32_e32 v40, 0x28a8, v20
	v_add_u32_e32 v41, 0x2cb0, v20
	v_add_u32_e32 v42, 0x2cb8, v20
	s_movk_i32 s64, 0xba3
	s_mov_b32 s65, 0xb000
	s_mov_b32 s66, 0x16000
	s_mov_b32 s67, 0x21000
	s_mov_b32 s16, 0x2c000
	s_mov_b32 s68, 0x37000
	s_mov_b32 s69, 0x42000
	s_mov_b32 s19, 0x4d000
	s_mov_b32 s20, 0x58000
	s_mov_b32 s21, 0x63000
	s_mov_b32 s70, 0x6e000
	s_mov_b32 s23, 0x79000
	s_mov_b32 s24, 0x84000
	s_mov_b32 s25, 0x8f000
	s_mov_b32 s26, 0x9a000
	s_mov_b32 s27, 0xa5000
	s_mov_b32 s71, 0x107ff
	v_lshlrev_b32_e32 v2, 2, v44
	v_add_u32_e32 v43, 0x30c0, v20
	v_add_u32_e32 v44, 0x30c8, v20
	v_add_u32_e32 v45, 0x34d0, v20
	v_add_u32_e32 v46, 0x34d8, v20
	v_mov_b32_e32 v47, 6
	v_mov_b32_e32 v132, 1
	v_mov_b32_e32 v133, 8
	v_mov_b32_e32 v134, 7
	s_branch .Lcvp14_58
